# norm1 (l>0) and final norm copy the MoE tile table from lds+0x20000 (left by moe_gu of the previous layer) instead of rebuilding it from the global counts (on top of v47)
# speedup vs baseline: 1.0135x; 1.0004x over previous
.LBB0_342:
	s_andn2_b64 vcc, exec, s[2:3]
	s_cbranch_vccnz .LBB0_506
	v_readlane_b32 s2, v255, 33
	s_cmp_lg_u32 s2, 0
	s_cselect_b64 s[24:25], -1, 0
	s_cmp_eq_u32 s2, 0
	v_readlane_b32 s3, v255, 34
	v_mbcnt_lo_u32_b32 v214, -1, 0
	v_mbcnt_hi_u32_b32 v214, -1, v214
	v_lshl_add_u32 v215, s43, 6, v214
	s_cbranch_scc1 .LBB0_368
	v_lshlrev_b32_e32 v0, 2, v215
	v_add_u32_e32 v1, 0x20000, v0
	ds_read_b32 v1, v1
	s_waitcnt lgkmcnt(0)
	ds_write_b32 v0, v1
	s_waitcnt lgkmcnt(0)
	s_barrier

.LBB0_1727:
	v_readlane_b32 s0, v250, 4
	v_mov_b32 v0, s0
	ds_read_b32 v0, v0 offset:8
	v_mov_b32 v1, s0
	ds_read_b32 v1, v1 offset:12
	s_waitcnt lgkmcnt(0)
	v_readfirstlane_b32 s0, v0
	s_cmp_lt_i32 s0, 44
	v_readfirstlane_b32 s21, v1
	s_cselect_b64 s[0:1], -1, 0
	s_cmp_gt_i32 s21, 43
	s_cselect_b64 s[2:3], -1, 0
	s_and_b64 s[0:1], s[0:1], s[2:3]
	s_and_b64 vcc, exec, s[0:1]
	s_cbranch_vccz .LBB0_1826
	v_mbcnt_lo_u32_b32 v2, -1, 0
	v_mbcnt_hi_u32_b32 v2, -1, v2
	v_lshl_add_u32 v3, s43, 6, v2
	s_nop 0
	v_readlane_b32 s10, v255, 17
	v_readlane_b32 s38, v252, 10
	v_readlane_b32 s11, v255, 18
	v_readlane_b32 s39, v252, 11
	v_lshlrev_b32_e32 v0, 2, v3
	v_add_u32_e32 v1, 0x20000, v0
	ds_read_b32 v1, v1
	s_waitcnt lgkmcnt(0)
	ds_write_b32 v0, v1
	s_add_i32 s0, s37, 0x3fff
	s_ashr_i32 s1, s0, 31
	v_readlane_b32 s2, v252, 0
	s_xor_b32 s1, s1, s2
	s_sub_i32 s2, 0xffffc001, s37
	s_max_i32 s0, s0, s2
	v_readlane_b32 s2, v252, 33
	s_mul_hi_u32 s2, s0, s2
	v_readlane_b32 s5, v252, 34
	s_mul_i32 s3, s2, s5
	s_sub_i32 s0, s0, s3
	s_add_i32 s3, s2, 1
	s_sub_i32 s4, s0, s5
	s_cmp_ge_u32 s0, s5
	s_cselect_b32 s2, s3, s2
	s_cselect_b32 s0, s4, s0
	s_add_i32 s3, s2, 1
	s_cmp_ge_u32 s0, s5
	s_cselect_b32 s0, s3, s2
	s_xor_b32 s0, s0, s1
	s_sub_i32 s0, s0, s1
	s_mul_i32 s8, s0, s94
	s_add_i32 s1, s8, 0x800
	s_add_i32 s0, s1, s0
	s_min_i32 s2, s0, 0x4800
	s_add_i32 s0, s1, s43
	s_cmp_ge_i32 s0, s2
	s_waitcnt lgkmcnt(0)
	s_barrier
	s_cbranch_scc1 .LBB0_1772
	s_min_i32 s1, s1, 0x47ff
	s_load_dwordx4 s[4:7], s[10:11], 0x118
	s_addk_i32 s1, 0xf800
	s_add_i32 s3, s2, -1
	s_lshr_b32 s1, s1, 11
	v_lshlrev_b32_e32 v80, 2, v2
	s_cmp_gt_i32 s8, -1
	v_ashrrev_i32_e32 v81, 31, v80
	s_cselect_b32 s33, s1, 8
	v_lshlrev_b64 v[48:49], 2, v[80:81]
	s_add_i32 s1, s33, 27
	s_waitcnt lgkmcnt(0)
	v_lshl_add_u64 v[16:17], s[4:5], 0, v[48:49]
	s_mul_hi_u32 s5, s1, 0x6000
	s_mulk_i32 s1, 0x6000
	s_add_u32 s4, s84, s1
	s_addc_u32 s5, s86, s5
	s_add_i32 s1, s0, 8
	global_load_dwordx4 v[0:3], v[16:17], off
	global_load_dwordx4 v[4:7], v[16:17], off offset:1024
	global_load_dwordx4 v[8:11], v[16:17], off offset:2048
	global_load_dwordx4 v[12:15], v[16:17], off offset:3072
	v_lshl_add_u64 v[16:17], s[4:5], 0, v[48:49]
	s_min_i32 s4, s1, s3
	s_ashr_i32 s5, s4, 31
	s_lshl_b64 s[4:5], s[4:5], 4
	s_add_u32 s10, s38, s4
	s_addc_u32 s11, s39, s5
	s_add_u32 s4, s90, s4
	v_mov_b32_e32 v106, 0
	s_addc_u32 s5, s91, s5
	s_ashr_i32 s1, s0, 31
	global_load_dwordx4 v[40:43], v106, s[10:11]
	global_load_dwordx4 v[32:35], v106, s[4:5]
	s_lshl_b64 s[4:5], s[0:1], 4
	s_add_u32 s10, s38, s4
	s_mov_b64 s[16:17], 0x5000
	s_movk_i32 s9, 0x5000
	s_addc_u32 s11, s39, s5
	v_lshl_add_u64 v[50:51], v[16:17], 0, s[16:17]
	s_add_u32 s4, s90, s4
	v_add_co_u32_e32 v52, vcc, s9, v16
	s_addc_u32 s5, s91, s5
	global_load_dwordx4 v[44:47], v106, s[10:11]
	global_load_dwordx4 v[36:39], v106, s[4:5]
	v_addc_co_u32_e32 v53, vcc, 0, v17, vcc
	global_load_dwordx4 v[16:19], v[50:51], off offset:1024
	global_load_dwordx4 v[20:23], v[50:51], off offset:2048
	global_load_dwordx4 v[24:27], v[52:53], off
	global_load_dwordx4 v[28:31], v[50:51], off offset:3072
	s_add_i32 s24, s43, s8
	s_lshl_b64 s[0:1], s[0:1], 11
	s_add_u32 s0, s60, s0
	v_lshlrev_b64 v[50:51], 1, v[80:81]
	v_readlane_b32 s10, v250, 5
	s_addc_u32 s1, s61, s1
	s_mov_b64 s[4:5], 0x3ad38000
	v_readlane_b32 s11, v250, 6
	v_lshl_add_u64 v[84:85], s[6:7], 0, v[48:49]
	v_lshl_add_u64 v[48:49], s[0:1], 0, v[50:51]
	s_mov_b32 s19, 0
	s_mov_b32 s20, 0x3e000000
	v_mov_b32_e32 v107, 0x358637bd
	s_mov_b32 s34, 0x800000
	s_mov_b64 s[22:23], 0x8000
	v_lshl_add_u64 v[82:83], s[10:11], 0, v[50:51]
	v_lshl_add_u64 v[86:87], v[48:49], 0, s[4:5]
	v_mov_b32_e32 v108, 0x3a800000
	s_waitcnt vmcnt(6)
	v_readfirstlane_b32 s12, v32
	v_readfirstlane_b32 s13, v33
	v_readfirstlane_b32 s14, v34
	v_readfirstlane_b32 s15, v35
	s_waitcnt vmcnt(4)
	v_readfirstlane_b32 s4, v36
	v_readfirstlane_b32 s5, v37
	v_readfirstlane_b32 s6, v38
	v_readfirstlane_b32 s7, v39
	s_branch .LBB0_1754
